# stack16
# speedup vs baseline: 1.0006x; 1.0006x over previous
.LBB3_56:
	s_or_b64 exec, exec, s[24:25]
	s_add_i32 s34, s34, 1
	s_add_i32 s18, s18, 4
	s_xor_b64 s[20:21], s[20:21], -1
	s_cmp_eq_u32 s34, 25
	v_add_u32_e32 v230, 0xfb000000, v240
	v_mov_b64_e32 v[132:133], v[52:53]
	v_mov_b64_e32 v[134:135], v[50:51]
	v_mov_b64_e32 v[136:137], v[56:57]
	v_mov_b64_e32 v[138:139], v[54:55]
	v_mov_b64_e32 v[140:141], v[44:45]
	v_mov_b64_e32 v[142:143], v[42:43]
	v_mov_b64_e32 v[144:145], v[48:49]
	v_mov_b64_e32 v[146:147], v[46:47]
	v_mov_b64_e32 v[156:157], v[36:37]
	v_mov_b64_e32 v[158:159], v[34:35]
	v_mov_b64_e32 v[160:161], v[40:41]
	v_mov_b64_e32 v[162:163], v[38:39]
	v_mov_b64_e32 v[166:167], v[28:29]
	v_mov_b64_e32 v[168:169], v[26:27]
	v_mov_b64_e32 v[170:171], v[32:33]
	v_mov_b64_e32 v[172:173], v[30:31]
	v_mov_b64_e32 v[174:175], v[20:21]
	v_mov_b64_e32 v[176:177], v[18:19]
	v_mov_b64_e32 v[178:179], v[24:25]
	v_mov_b64_e32 v[180:181], v[22:23]
	v_mov_b64_e32 v[190:191], v[12:13]
	v_mov_b64_e32 v[192:193], v[10:11]
	v_mov_b64_e32 v[194:195], v[16:17]
	v_mov_b64_e32 v[196:197], v[14:15]
	v_mov_b64_e32 v[206:207], v[4:5]
	v_mov_b64_e32 v[208:209], v[2:3]
	v_mov_b64_e32 v[210:211], v[8:9]
	v_mov_b64_e32 v[212:213], v[6:7]
	v_mov_b64_e32 v[52:53], v[88:89]
	v_mov_b64_e32 v[50:51], v[86:87]
	v_mov_b64_e32 v[56:57], v[84:85]
	v_mov_b64_e32 v[54:55], v[82:83]
	v_mov_b64_e32 v[44:45], v[80:81]
	v_mov_b64_e32 v[42:43], v[78:79]
	v_mov_b64_e32 v[48:49], v[76:77]
	v_mov_b64_e32 v[46:47], v[74:75]
	v_mov_b64_e32 v[36:37], v[72:73]
	v_mov_b64_e32 v[34:35], v[70:71]
	v_mov_b64_e32 v[40:41], v[68:69]
	v_mov_b64_e32 v[38:39], v[66:67]
	v_mov_b64_e32 v[28:29], v[228:229]
	v_mov_b64_e32 v[26:27], v[226:227]
	v_mov_b64_e32 v[32:33], v[224:225]
	v_mov_b64_e32 v[30:31], v[222:223]
	v_mov_b64_e32 v[20:21], v[220:221]
	v_mov_b64_e32 v[18:19], v[218:219]
	v_mov_b64_e32 v[24:25], v[216:217]
	v_mov_b64_e32 v[22:23], v[214:215]
	v_mov_b64_e32 v[12:13], v[204:205]
	v_mov_b64_e32 v[10:11], v[202:203]
	v_mov_b64_e32 v[16:17], v[200:201]
	v_mov_b64_e32 v[14:15], v[198:199]
	v_mov_b64_e32 v[4:5], v[188:189]
	v_mov_b64_e32 v[2:3], v[186:187]
	v_mov_b64_e32 v[8:9], v[184:185]
	v_mov_b64_e32 v[6:7], v[182:183]
	v_mov_b64_e32 v[148:149], v[124:125]
	v_mov_b64_e32 v[150:151], v[128:129]
	v_mov_b64_e32 v[152:153], v[126:127]
	v_mov_b64_e32 v[154:155], v[130:131]
	s_waitcnt lgkmcnt(0)
	s_barrier
	s_cbranch_scc1 .LBB3_58
	s_branch .LBB3_8
